# rope frequency by binary exponentiation (5 conditional f64 multiplies instead of a divergent loop of up to 31)
# baseline (speedup 1.0000x reference)
.LBB0_56:
	s_or_b64 exec, exec, s[8:9]
	s_mov_b32 s0, 0x80000
	v_cmp_gt_i32_e32 vcc, s0, v0
	s_and_saveexec_b64 s[8:9], vcc
	s_cbranch_execz .LBB0_63
	s_add_u32 s10, s78, 0x100000
	s_addc_u32 s11, s79, 0
	s_add_u32 s12, s78, 0x300000
	v_and_b32_e32 v4, 31, v28
	s_mov_b32 s16, 0x24115d99
	s_mov_b32 s18, 0x6dc9c883
	s_addc_u32 s13, s79, 0
	v_cmp_ne_u32_e32 vcc, 0, v4
	s_mov_b64 s[14:15], 0
	s_mov_b32 s17, 0x3fe7ff22
	s_mov_b32 s19, 0x3fc45f30
	s_mov_b32 s5, 0x7ffff
	v_mov_b64_e32 v[14:15], 1.0
	s_mov_b32 s22, 0x24115d99
	s_mov_b32 s23, 0x3fe7ff22
	v_and_b32_e32 v1, 1, v4
	v_mul_f64 v[16:17], v[14:15], s[22:23]
	v_cmp_ne_u32_e32 vcc, 0, v1
	s_nop 1
	v_cndmask_b32_e32 v14, v14, v16, vcc
	v_cndmask_b32_e32 v15, v15, v17, vcc
	s_mov_b32 s22, 0x3c1c381d
	s_mov_b32 s23, 0x3fe1feb3
	v_and_b32_e32 v1, 2, v4
	v_mul_f64 v[16:17], v[14:15], s[22:23]
	v_cmp_ne_u32_e32 vcc, 0, v1
	s_nop 1
	v_cndmask_b32_e32 v14, v14, v16, vcc
	v_cndmask_b32_e32 v15, v15, v17, vcc
	s_mov_b32 s22, 0x6248490c
	s_mov_b32 s23, 0x3fd43d13
	v_and_b32_e32 v1, 4, v4
	v_mul_f64 v[16:17], v[14:15], s[22:23]
	v_cmp_ne_u32_e32 vcc, 0, v1
	s_nop 1
	v_cndmask_b32_e32 v14, v14, v16, vcc
	v_cndmask_b32_e32 v15, v15, v17, vcc
	s_mov_b32 s22, 0x99999992
	s_mov_b32 s23, 0x3fb99999
	v_and_b32_e32 v1, 8, v4
	v_mul_f64 v[16:17], v[14:15], s[22:23]
	v_cmp_ne_u32_e32 vcc, 0, v1
	s_nop 1
	v_cndmask_b32_e32 v14, v14, v16, vcc
	v_cndmask_b32_e32 v15, v15, v17, vcc
	s_mov_b32 s22, 0x47ae146f
	s_mov_b32 s23, 0x3f847ae1
	v_and_b32_e32 v1, 16, v4
	v_mul_f64 v[16:17], v[14:15], s[22:23]
	v_cmp_ne_u32_e32 vcc, 0, v1
	s_nop 1
	v_cndmask_b32_e32 v14, v14, v16, vcc
	v_cndmask_b32_e32 v15, v15, v17, vcc
	s_waitcnt vmcnt(0)
	s_branch .LBB0_58
